# P10 down-GEMM: B rows permuted on the source side so each lane owns 16 contiguous fp8 output columns; 16 dwordx2 epilogue stores merged into 8 dwordx4
# speedup vs baseline: 1.0173x; 1.0081x over previous
; #define PG8_STAGE(bufoff, gbase, voff) do { _Pragma("unroll") for (int _i = 0; _i < 2; ++_i) { unsigned _vo = (voff)[_i]; asm volatile("" : "+v"(_vo)); \
;         __builtin_amdgcn_global_load_lds((const unsigned*)((const char*)(gbase) + _vo), (LAS unsigned*)(lds + (bufoff) + ldsw + _i * 8192), 16, 0, 0); } } while (0)
; #define PG8_STAGE_A(bufoff, gbase, h, go) do { if constexpr (Sched::GATHER) { PG8_STAGE(bufoff, gbase, go[h]); } else { PG8_STAGE(bufoff, (gbase) + (h) * hstep, voffA); } } while (0)
; #define PG8_WAIT_V(n) asm volatile("s_waitcnt vmcnt(" #n ")" ::: "memory")
; #define PG8_BAR __builtin_amdgcn_s_barrier()
;     __device__ __forceinline__ void prefetch(const Unit& u) const { if (u.e == 0) rs.prefetch(u); else cs.prefetch(u); }
;     ...
;     for (int i = 0; i < 2; ++i) { int R, C; stage_rc(tid * 16 + i * 8192, R, C); const int Rb = Epi::PERM ? ((R & ~31) + perm32(R & 31)) : R;
;         voffA[i] = Sched::GATHER ? (unsigned)(C * 2) : (unsigned)(R * KB + C * 2); voffB[i] = (unsigned)(Rb * KB + C * 2); }
;     const size_t kstep = (size_t)(BK * 2);
;     const size_t hstep = (size_t)HALF * KB;
;     const unsigned ldsw = (unsigned)wid * 1024u;
;     const int aoff = lds_byte(wr * 64 + fr, fq * 8), boff = lds_byte(wc * 32 + fr, fq * 8);
;     ...
;     Unit cur, nxt; int ui = 0;
;     if (!S.next(0, cur)) return;
;     Acc acc;
; #pragma unroll
;     for (int a = 0; a < 2; ++a)
; #pragma unroll
;         for (int b = 0; b < 2; ++b)
; #pragma unroll
;             for (int m = 0; m < 4; ++m)
; #pragma unroll
;                 for (int n = 0; n < 2; ++n) acc[a][b][m][n] = (f32x4){0.f, 0.f, 0.f, 0.f};
;     bf16x8 At[4][2], B0[2][2], B1[2][2];
;     const char* cA = cur.a; const char* cB = cur.b;
;     unsigned gc[2][2], gn[2][2];
;     if constexpr (Sched::GATHER) { S.gather(cur, voffA, gc); }
;     if constexpr (Epi::PREF) E.prefetch(cur);
;     PG8_STAGE(PG8_SB(0, 0), cB, voffB); PG8_STAGE(PG8_SB(0, 1), cB + hstep, voffB); PG8_STAGE_A(PG8_SA(0, 0), cA, 0, gc); PG8_STAGE_A(PG8_SA(0, 1), cA, 1, gc);
;     if (wr == 1) PG8_BAR;
;     PG8_WAIT_V(2); PG8_BAR;
;     PG8_STAGE(PG8_SB(1, 0), cB + kstep, voffB); PG8_STAGE_A(PG8_SA(1, 0), cA + kstep, 0, gc); PG8_STAGE(PG8_SB(1, 1), cB + hstep + kstep, voffB);
;     PG8_WAIT_V(6); PG8_BAR;
.LBB5_1668:
	s_add_u32 s27, s22, 0x68000000
	s_addc_u32 s29, s23, 0
	v_lshrrev_b32_e32 v1, 4, v0
	v_xor_b32_e32 v1, v1, v0
	s_add_u32 s38, s22, 0x28000000
	v_and_b32_e32 v1, 7, v1
	s_addc_u32 s39, s23, 0
	s_lshr_b32 s11, s3, 21
	v_lshlrev_b32_e32 v3, 4, v1
	v_lshrrev_b32_e32 v6, 3, v0
	s_lshl_b32 s3, s11, 19
	v_and_b32_e32 v5, 3, v6
	v_bfe_u32 v7, v6, 2, 2
	s_add_u32 s18, s27, s3
	v_lshl_or_b32 v5, v7, 4, v5
	v_bfe_u32 v7, v6, 4, 1
	s_addc_u32 s19, s29, 0
	s_lshl_b32 s2, s2, 22
	s_lshl_b32 s3, s56, 19
	v_lshl_or_b32 v5, v7, 2, v5
	v_bfe_u32 v7, v6, 5, 1
	v_lshl_or_b32 v7, v7, 6, v5
	s_add_i32 s3, s3, s2
	v_lshl_or_b32 v1, v6, 11, v3
	v_or_b32_e32 v4, 64, v6
	s_add_u32 s34, s38, s3
	s_movk_i32 s2, 0x70
	s_addc_u32 s35, s39, 0
	s_movk_i32 s2, 0x60
	s_lshr_b32 s7, s8, 6
	v_lshl_or_b32 v140, v7, 11, v3
	v_or_b32_e32 v5, 0x80, v7
	s_lshl_b32 s40, s7, 10
	v_lshl_or_b32 v141, v4, 11, v3
	v_lshl_or_b32 v142, v5, 11, v3
	s_add_i32 s41, s40, 0
	v_mov_b32_e32 v3, v140
	s_add_i32 m0, s41, 0x10000
	s_lshr_b32 s6, s8, 8
	global_load_lds_dwordx4 v3, s[34:35]
	v_mov_b32_e32 v3, v142
	s_add_i32 m0, s41, 0x12000
	s_add_u32 s2, s34, 0x4000
	global_load_lds_dwordx4 v3, s[34:35]
	v_mov_b32_e32 v3, v140
	s_addc_u32 s3, s35, 0
	s_add_i32 m0, s41, 0x14000
	s_add_i32 s42, s41, 0x2000
	global_load_lds_dwordx4 v3, s[2:3]
	v_mov_b32_e32 v3, v142
	s_add_i32 m0, s41, 0x16000
	s_mov_b32 s57, 0
	global_load_lds_dwordx4 v3, s[2:3]
	v_mov_b32_e32 v3, v1
	s_mov_b32 m0, s41
	s_add_u32 s2, s18, 0x40000
	global_load_lds_dwordx4 v3, s[18:19]
	v_mov_b32_e32 v3, v141
	s_mov_b32 m0, s42
	s_addc_u32 s3, s19, 0
	global_load_lds_dwordx4 v3, s[18:19]
	s_add_i32 s43, s41, 0x4000
	v_mov_b32_e32 v3, v1
	s_mov_b32 m0, s43
	s_add_i32 s44, s41, 0x6000
	global_load_lds_dwordx4 v3, s[2:3]
	v_mov_b32_e32 v3, v141
	s_mov_b32 m0, s44
	s_cmp_eq_u32 s6, 1
	global_load_lds_dwordx4 v3, s[2:3]
	s_cselect_b64 s[2:3], -1, 0
	s_cmp_lg_u32 s6, 1
	s_cbranch_scc1 .LBB5_1670
	s_barrier
.LBB5_1670:
	s_add_u32 s4, s22, 0x8a000000
	s_addc_u32 s5, s23, 0
	s_lshl_b32 s45, s6, 6
	s_lshl_b32 s9, s6, 13
	s_lshl_b32 s6, s7, 5
	v_mov_b32_e32 v138, v140
	v_mov_b32_e32 v139, 0
	s_and_b32 s46, s6, 0x60
	s_waitcnt vmcnt(2)
	s_barrier
	s_mov_b64 s[6:7], 0x80
	v_lshl_add_u64 v[4:5], s[34:35], 0, v[138:139]
	s_add_i32 m0, s41, 0x18000
	v_lshl_add_u64 v[4:5], v[4:5], 0, s[6:7]
	v_mov_b32_e32 v138, v142
	global_load_lds_dwordx4 v[4:5], off
	s_add_i32 m0, s41, 0x1a000
	v_lshl_add_u64 v[4:5], s[34:35], 0, v[138:139]
	v_lshl_add_u64 v[4:5], v[4:5], 0, s[6:7]
	v_mov_b32_e32 v138, v1
	global_load_lds_dwordx4 v[4:5], off
	s_add_i32 s47, s41, 0x8000
	v_lshl_add_u64 v[4:5], s[18:19], 0, v[138:139]
	v_lshl_add_u64 v[4:5], v[4:5], 0, s[6:7]
	s_mov_b32 m0, s47
	v_mov_b32_e32 v138, v141
	s_lshl_b32 s10, s46, 7
	global_load_lds_dwordx4 v[4:5], off
	s_add_i32 s48, s41, 0xa000
	v_lshl_add_u64 v[4:5], s[18:19], 0, v[138:139]
	v_lshl_add_u64 v[4:5], v[4:5], 0, s[6:7]
	s_mov_b32 m0, s48
	s_add_u32 s12, s34, 0x4080
	v_mov_b32_e32 v3, v140
	global_load_lds_dwordx4 v[4:5], off
	s_addc_u32 s13, s35, 0
	s_add_i32 m0, s41, 0x1c000
	v_bfe_u32 v144, v0, 4, 2
	global_load_lds_dwordx4 v3, s[12:13]
	v_mov_b32_e32 v3, v142
	s_add_i32 m0, s41, 0x1e000
	v_and_b32_e32 v143, 15, v0
	global_load_lds_dwordx4 v3, s[12:13]
	v_lshrrev_b32_e32 v3, 1, v143
	v_xor_b32_e32 v3, v3, v144
	v_lshlrev_b32_e32 v3, 4, v3
	v_lshl_or_b32 v3, v143, 7, v3
	v_or_b32_e32 v4, s9, v3
	s_movk_i32 s9, 0x3c0
	s_cmpk_lt_u32 s8, 0x100
	v_or_b32_e32 v145, s10, v3
	s_waitcnt vmcnt(6)
	s_cselect_b64 s[8:9], -1, 0
	s_lshl_b32 s10, s46, 2
	s_add_i32 s49, s10, 0
	s_add_i32 s50, 0, 0x10000
	s_add_i32 s51, 0, 0x14000
	s_add_i32 s49, s49, 0x20800
	v_add_u32_e32 v146, s50, v145
	v_add_u32_e32 v147, s51, v145
	v_add_u32_e32 v148, 0, v4
	v_mov_b32_e32 v149, 0x7c7c7c7c
	v_lshlrev_b32_e32 v150, 2, v0
	s_mov_b32 s54, 0
	s_barrier
	s_branch .LBB5_1673

; #define PG8_STAGE(bufoff, gbase, voff) do { _Pragma("unroll") for (int _i = 0; _i < 2; ++_i) { unsigned _vo = (voff)[_i]; asm volatile("" : "+v"(_vo)); \
;         __builtin_amdgcn_global_load_lds((const unsigned*)((const char*)(gbase) + _vo), (LAS unsigned*)(lds + (bufoff) + ldsw + _i * 8192), 16, 0, 0); } } while (0)
; #define PG8_STAGE_A(bufoff, gbase, h, go) do { if constexpr (Sched::GATHER) { PG8_STAGE(bufoff, gbase, go[h]); } else { PG8_STAGE(bufoff, (gbase) + (h) * hstep, voffA); } } while (0)
; #define PG8_WAIT_V(n) asm volatile("s_waitcnt vmcnt(" #n ")" ::: "memory")
; #define PG8_WAIT_L(n) asm volatile("s_waitcnt lgkmcnt(" #n ")" ::: "memory")
;     ...
;         for (int t = 0; t < nt; t += 2) {
;             const bool last = (t == nt - 2);
;             if constexpr (Epi::MIDK) { if (t == nt / 2) { int fr_e = fr; asm volatile("" : "+v"(fr_e)); E.midk(acc, cur, wr, fr_e); } }
;             const char* a1 = cA + (size_t)(t + 1) * kstep;
;             const char* a2 = last ? nA : cA + (size_t)(t + 2) * kstep; const char* b2 = last ? nB : cB + (size_t)(t + 2) * kstep;
;             const char* a3 = a2 + kstep; const char* b3 = b2 + kstep;
;             PG8_LDB(B0, 0, 0); PG8_LDB(B1, 0, 1); PG8_SCHED; PG8_LDA(At, 0, 0); PG8_STAGE_A(PG8_SA(1, 1), a1, 1, gc);
;             if constexpr (Sched::GATHER) { if (last) {
; #pragma unroll
;                 for (int h = 0; h < 2; ++h)
; #pragma unroll
;                     for (int i = 0; i < 2; ++i) gc[h][i] = gn[h][i]; } }
;             PG8_WAIT_V(8); PG8_WAIT_L(0); PG8_BAR; PG8_MMA(0, 0, At, B0); PG8_MMA(0, 1, At, B1); PG8_BAR; PG8_SCHED;
;             PG8_LDA(At, 0, 1); PG8_STAGE(PG8_SB(0, 0), b2, voffB); PG8_STAGE(PG8_SB(0, 1), b2 + hstep, voffB); PG8_STAGE_A(PG8_SA(0, 0), a2, 0, gc);
;             PG8_WAIT_V(8); PG8_WAIT_L(0); PG8_BAR; PG8_MMA(1, 0, At, B0); PG8_MMA(1, 1, At, B1); PG8_BAR; PG8_SCHED;
;             PG8_LDB(B0, 1, 0); PG8_LDB(B1, 1, 1); PG8_SCHED; PG8_LDA(At, 1, 0); PG8_STAGE_A(PG8_SA(0, 1), a2, 1, gc);
;             PG8_WAIT_V(8); PG8_WAIT_L(0); PG8_BAR; PG8_MMA(0, 0, At, B0); PG8_MMA(0, 1, At, B1); PG8_BAR; PG8_SCHED;
;             PG8_LDA(At, 1, 1); PG8_STAGE(PG8_SB(1, 0), b3, voffB); PG8_STAGE(PG8_SB(1, 1), b3 + hstep, voffB); PG8_STAGE_A(PG8_SA(1, 0), a3, 0, gc);
;             PG8_WAIT_V(8); PG8_WAIT_L(0); PG8_BAR; PG8_MMA(1, 0, At, B0); PG8_MMA(1, 1, At, B1); PG8_BAR; PG8_SCHED;
.LBB5_1678:
	ds_read_b128 v[130:133], v146
	ds_read_b128 v[152:155], v146 offset:2048
	v_xor_b32_e32 v146, 64, v146
	ds_read_b128 v[134:137], v146
	ds_read_b128 v[156:159], v146 offset:2048
	v_xor_b32_e32 v146, 64, v146
	ds_read_b128 v[160:163], v147
	ds_read_b128 v[168:171], v147 offset:2048
	v_xor_b32_e32 v147, 64, v147
	ds_read_b128 v[164:167], v147
	ds_read_b128 v[172:175], v147 offset:2048
	v_xor_b32_e32 v147, 64, v147
	s_add_u32 s34, s18, 0xfffc0080
	s_addc_u32 s35, s19, -1
	s_cmp_eq_u32 s64, 12
	s_cselect_b32 s35, s58, s35
	s_cselect_b32 s34, s59, s34
	s_cselect_b32 s37, s60, s63
	s_cselect_b32 s36, s61, s62
	v_mov_b32_e32 v138, v1
	ds_read_b128 v[176:179], v148
	ds_read_b128 v[184:187], v148 offset:2048
	ds_read_b128 v[200:203], v148 offset:4096
	ds_read_b128 v[208:211], v148 offset:6144
	v_xor_b32_e32 v148, 64, v148
	ds_read_b128 v[180:183], v148
	ds_read_b128 v[188:191], v148 offset:2048
	ds_read_b128 v[204:207], v148 offset:4096
	ds_read_b128 v[212:215], v148 offset:6144
	s_add_u32 s98, s62, 0x3f80
	s_addc_u32 s99, s63, 0
	s_add_i32 s100, s40, 0x1c000
	v_mov_b32_e32 v138, v140
	s_mov_b32 m0, s100
	s_nop 0
	global_load_lds_dwordx4 v138, s[98:99]
	v_mov_b32_e32 v138, v142
	s_add_i32 m0, s100, 0x2000
	s_nop 0
	global_load_lds_dwordx4 v138, s[98:99]
	v_mov_b32_e32 v138, v1
	s_add_i32 m0, s41, 0xc000
	s_nop 0
	global_load_lds_dwordx4 v138, s[18:19]
	v_mov_b32_e32 v138, v141
	s_add_i32 m0, s41, 0xe000
	s_nop 0
	global_load_lds_dwordx4 v138, s[18:19]
	s_waitcnt vmcnt(8)
	s_waitcnt lgkmcnt(0)
	s_barrier
	s_setprio 1
	s_waitcnt lgkmcnt(0)
	v_mfma_scale_f32_16x16x128_f8f6f4 v[126:129], v[130:137], v[176:183], v[126:129], v149, v149 op_sel_hi:[0,0,0]
	v_mfma_scale_f32_16x16x128_f8f6f4 v[122:125], v[152:159], v[176:183], v[122:125], v149, v149 op_sel_hi:[0,0,0]
	v_mfma_scale_f32_16x16x128_f8f6f4 v[118:121], v[130:137], v[184:191], v[118:121], v149, v149 op_sel_hi:[0,0,0]
	v_mfma_scale_f32_16x16x128_f8f6f4 v[114:117], v[152:159], v[184:191], v[114:117], v149, v149 op_sel_hi:[0,0,0]
	v_mfma_scale_f32_16x16x128_f8f6f4 v[110:113], v[130:137], v[200:207], v[110:113], v149, v149 op_sel_hi:[0,0,0]
	v_mfma_scale_f32_16x16x128_f8f6f4 v[106:109], v[152:159], v[200:207], v[106:109], v149, v149 op_sel_hi:[0,0,0]
	v_mfma_scale_f32_16x16x128_f8f6f4 v[102:105], v[130:137], v[208:215], v[102:105], v149, v149 op_sel_hi:[0,0,0]
	v_mfma_scale_f32_16x16x128_f8f6f4 v[98:101], v[152:159], v[208:215], v[98:101], v149, v149 op_sel_hi:[0,0,0]
	s_setprio 0
	s_setprio 1
	v_mfma_scale_f32_16x16x128_f8f6f4 v[192:195], v[160:167], v[176:183], v[70:73], v149, v149 op_sel_hi:[0,0,0]
	v_mfma_scale_f32_16x16x128_f8f6f4 v[176:179], v[168:175], v[176:183], v[66:69], v149, v149 op_sel_hi:[0,0,0]
	v_mfma_scale_f32_16x16x128_f8f6f4 v[180:183], v[160:167], v[184:191], v[54:57], v149, v149 op_sel_hi:[0,0,0]
	v_mfma_scale_f32_16x16x128_f8f6f4 v[184:187], v[168:175], v[184:191], v[50:53], v149, v149 op_sel_hi:[0,0,0]
	v_mfma_scale_f32_16x16x128_f8f6f4 v[188:191], v[160:167], v[200:207], v[46:49], v149, v149 op_sel_hi:[0,0,0]
	v_mfma_scale_f32_16x16x128_f8f6f4 v[200:203], v[168:175], v[200:207], v[42:45], v149, v149 op_sel_hi:[0,0,0]
	v_mfma_scale_f32_16x16x128_f8f6f4 v[204:207], v[160:167], v[208:215], v[38:41], v149, v149 op_sel_hi:[0,0,0]
	v_mfma_scale_f32_16x16x128_f8f6f4 v[208:211], v[168:175], v[208:215], v[34:37], v149, v149 op_sel_hi:[0,0,0]
	s_setprio 0
	s_barrier
	v_mov_b32_e32 v138, v140
	s_add_i32 s65, s50, s40
	s_nop 2
	ds_read_b128 v[38:41], v148 offset:16384
	ds_read_b128 v[46:49], v148 offset:18432
	ds_read_b128 v[54:57], v148 offset:20480
	ds_read_b128 v[70:73], v148 offset:22528
	v_xor_b32_e32 v148, 64, v148
	ds_read_b128 v[34:37], v148 offset:16384
	ds_read_b128 v[42:45], v148 offset:18432
	ds_read_b128 v[50:53], v148 offset:20480
	ds_read_b128 v[66:69], v148 offset:22528
	s_mov_b32 m0, s65
	s_nop 0
	global_load_lds_dwordx4 v138, s[36:37]
	v_mov_b32_e32 v138, v142
	s_add_i32 m0, s65, 0x2000
	s_nop 0
	global_load_lds_dwordx4 v138, s[36:37]
	v_mov_b32_e32 v138, v1
	s_mov_b32 m0, s41
	s_nop 0
	global_load_lds_dwordx4 v138, s[34:35]
	v_mov_b32_e32 v138, v141
	s_mov_b32 m0, s42
	s_nop 0
	global_load_lds_dwordx4 v138, s[34:35]
	s_waitcnt vmcnt(6)
	s_waitcnt lgkmcnt(0)
	s_barrier
	s_setprio 1
	s_waitcnt lgkmcnt(0)
	v_mfma_scale_f32_16x16x128_f8f6f4 v[94:97], v[130:137], v[34:41], v[94:97], v149, v149 op_sel_hi:[0,0,0]
	v_mfma_scale_f32_16x16x128_f8f6f4 v[90:93], v[152:159], v[34:41], v[90:93], v149, v149 op_sel_hi:[0,0,0]
	v_mfma_scale_f32_16x16x128_f8f6f4 v[86:89], v[130:137], v[42:49], v[86:89], v149, v149 op_sel_hi:[0,0,0]
	v_mfma_scale_f32_16x16x128_f8f6f4 v[82:85], v[152:159], v[42:49], v[82:85], v149, v149 op_sel_hi:[0,0,0]
	v_mfma_scale_f32_16x16x128_f8f6f4 v[78:81], v[130:137], v[50:57], v[78:81], v149, v149 op_sel_hi:[0,0,0]
	v_mfma_scale_f32_16x16x128_f8f6f4 v[74:77], v[152:159], v[50:57], v[74:77], v149, v149 op_sel_hi:[0,0,0]
	v_mfma_scale_f32_16x16x128_f8f6f4 v[212:215], v[130:137], v[66:73], v[62:65], v149, v149 op_sel_hi:[0,0,0]
	v_mfma_scale_f32_16x16x128_f8f6f4 v[216:219], v[152:159], v[66:73], v[58:61], v149, v149 op_sel_hi:[0,0,0]
	s_setprio 0
	s_setprio 1
	v_mfma_scale_f32_16x16x128_f8f6f4 v[220:223], v[160:167], v[34:41], v[30:33], v149, v149 op_sel_hi:[0,0,0]
	v_mfma_scale_f32_16x16x128_f8f6f4 v[224:227], v[168:175], v[34:41], v[26:29], v149, v149 op_sel_hi:[0,0,0]
	v_mfma_scale_f32_16x16x128_f8f6f4 v[228:231], v[160:167], v[42:49], v[22:25], v149, v149 op_sel_hi:[0,0,0]
	v_mfma_scale_f32_16x16x128_f8f6f4 v[232:235], v[168:175], v[42:49], v[18:21], v149, v149 op_sel_hi:[0,0,0]
	v_mfma_scale_f32_16x16x128_f8f6f4 v[236:239], v[160:167], v[50:57], v[14:17], v149, v149 op_sel_hi:[0,0,0]
	v_mfma_scale_f32_16x16x128_f8f6f4 v[240:243], v[168:175], v[50:57], v[10:13], v149, v149 op_sel_hi:[0,0,0]
	v_mfma_scale_f32_16x16x128_f8f6f4 v[244:247], v[160:167], v[66:73], v[6:9], v149, v149 op_sel_hi:[0,0,0]
	v_mfma_scale_f32_16x16x128_f8f6f4 v[248:251], v[168:175], v[66:73], v[2:5], v149, v149 op_sel_hi:[0,0,0]
	s_setprio 0
	s_barrier
; #define PG8_STAGE(bufoff, gbase, voff) do { _Pragma("unroll") for (int _i = 0; _i < 2; ++_i) { unsigned _vo = (voff)[_i]; asm volatile("" : "+v"(_vo)); \
;         __builtin_amdgcn_global_load_lds((const unsigned*)((const char*)(gbase) + _vo), (LAS unsigned*)(lds + (bufoff) + ldsw + _i * 8192), 16, 0, 0); } } while (0)
; #define PG8_STAGE_A(bufoff, gbase, h, go) do { if constexpr (Sched::GATHER) { PG8_STAGE(bufoff, gbase, go[h]); } else { PG8_STAGE(bufoff, (gbase) + (h) * hstep, voffA); } } while (0)
; #define PG8_LDA(dst, b, h) do { _Pragma("unroll") for (int m = 0; m < 4; ++m) _Pragma("unroll") for (int k = 0; k < 2; ++k) dst[m][k] = *(const LAS bf16x8*)(lds + PG8_SA(b, h) + aoff + m * 2048 + k * 1024); } while (0)
; #define PG8_LDB(dst, b, h) do { _Pragma("unroll") for (int n = 0; n < 2; ++n) _Pragma("unroll") for (int k = 0; k < 2; ++k) dst[n][k] = *(const LAS bf16x8*)(lds + PG8_SB(b, h) + boff + n * 2048 + k * 1024); } while (0)
; #define PG8_WAIT_V(n) asm volatile("s_waitcnt vmcnt(" #n ")" ::: "memory")
; #define PG8_WAIT_L(n) asm volatile("s_waitcnt lgkmcnt(" #n ")" ::: "memory")
; #define PG8_BAR __builtin_amdgcn_s_barrier()
; #define PG8_SCHED __builtin_amdgcn_sched_barrier(0)
;     ...
;             PG8_LDA(At, 0, 1); PG8_STAGE(PG8_SB(0, 0), b2, voffB); PG8_STAGE(PG8_SB(0, 1), b2 + hstep, voffB); PG8_STAGE_A(PG8_SA(0, 0), a2, 0, gc);
;             PG8_WAIT_V(8); PG8_WAIT_L(0); PG8_BAR; PG8_MMA(1, 0, At, B0); PG8_MMA(1, 1, At, B1); PG8_BAR; PG8_SCHED;
;             PG8_LDB(B0, 1, 0); PG8_LDB(B1, 1, 1); PG8_SCHED; PG8_LDA(At, 1, 0); PG8_STAGE_A(PG8_SA(0, 1), a2, 1, gc);
;             PG8_WAIT_V(8); PG8_WAIT_L(0); PG8_BAR; PG8_MMA(0, 0, At, B0); PG8_MMA(0, 1, At, B1); PG8_BAR; PG8_SCHED;
;             PG8_LDA(At, 1, 1); PG8_STAGE(PG8_SB(1, 0), b3, voffB); PG8_STAGE(PG8_SB(1, 1), b3 + hstep, voffB); PG8_STAGE_A(PG8_SA(1, 0), a3, 0, gc);
;             PG8_WAIT_V(8); PG8_WAIT_L(0); PG8_BAR; PG8_MMA(1, 0, At, B0); PG8_MMA(1, 1, At, B1); PG8_BAR; PG8_SCHED;
	s_add_i32 s65, 0, 0x18000
	s_add_i32 s68, 0, 0x1c000
	v_add_u32_e32 v14, s65, v145
	v_add_u32_e32 v18, s68, v145
	s_nop 0
	ds_read_b128 v[2:5], v14
	ds_read_b128 v[10:13], v14 offset:2048
	v_xor_b32_e32 v14, 64, v14
	ds_read_b128 v[6:9], v14
	ds_read_b128 v[14:17], v14 offset:2048
	ds_read_b128 v[130:133], v18
	ds_read_b128 v[152:155], v18 offset:2048
	v_xor_b32_e32 v18, 64, v18
	ds_read_b128 v[134:137], v18
	ds_read_b128 v[156:159], v18 offset:2048
	s_add_u32 s66, s34, 0x40000
	v_mov_b32_e32 v42, v1
	s_mov_b32 m0, s43
	ds_read_b128 v[18:21], v148 offset:32768
	ds_read_b128 v[26:29], v148 offset:34816
	ds_read_b128 v[34:37], v148 offset:36864
	ds_read_b128 v[58:61], v148 offset:38912
	v_xor_b32_e32 v148, 64, v148
	ds_read_b128 v[22:25], v148 offset:32768
	ds_read_b128 v[30:33], v148 offset:34816
	ds_read_b128 v[38:41], v148 offset:36864
	ds_read_b128 v[62:65], v148 offset:38912
	s_addc_u32 s67, s35, 0
	s_add_u32 s98, s36, 0x4000
	s_addc_u32 s99, s37, 0
	s_add_i32 s100, s51, s40
	v_mov_b32_e32 v42, v140
	s_mov_b32 m0, s100
	s_nop 0
	global_load_lds_dwordx4 v42, s[98:99]
	v_mov_b32_e32 v42, v142
	s_add_i32 m0, s100, 0x2000
	s_nop 0
	global_load_lds_dwordx4 v42, s[98:99]
	v_mov_b32_e32 v42, v1
	s_mov_b32 m0, s43
	s_nop 0
	global_load_lds_dwordx4 v42, s[66:67]
	v_mov_b32_e32 v42, v141
	s_mov_b32 m0, s44
	s_nop 0
	global_load_lds_dwordx4 v42, s[66:67]
	s_waitcnt vmcnt(8)
	s_waitcnt lgkmcnt(0)
	s_barrier
	s_setprio 1
	s_waitcnt lgkmcnt(0)
	v_mfma_scale_f32_16x16x128_f8f6f4 v[126:129], v[2:9], v[18:25], v[126:129], v149, v149 op_sel_hi:[0,0,0]
	v_mfma_scale_f32_16x16x128_f8f6f4 v[122:125], v[10:17], v[18:25], v[122:125], v149, v149 op_sel_hi:[0,0,0]
	v_mfma_scale_f32_16x16x128_f8f6f4 v[118:121], v[2:9], v[26:33], v[118:121], v149, v149 op_sel_hi:[0,0,0]
	v_mfma_scale_f32_16x16x128_f8f6f4 v[114:117], v[10:17], v[26:33], v[114:117], v149, v149 op_sel_hi:[0,0,0]
	v_mfma_scale_f32_16x16x128_f8f6f4 v[110:113], v[2:9], v[34:41], v[110:113], v149, v149 op_sel_hi:[0,0,0]
	v_mfma_scale_f32_16x16x128_f8f6f4 v[106:109], v[10:17], v[34:41], v[106:109], v149, v149 op_sel_hi:[0,0,0]
	v_mfma_scale_f32_16x16x128_f8f6f4 v[102:105], v[2:9], v[58:65], v[102:105], v149, v149 op_sel_hi:[0,0,0]
	v_mfma_scale_f32_16x16x128_f8f6f4 v[98:101], v[10:17], v[58:65], v[98:101], v149, v149 op_sel_hi:[0,0,0]
	s_setprio 0
	s_setprio 1
	v_mfma_scale_f32_16x16x128_f8f6f4 v[70:73], v[130:137], v[18:25], v[192:195], v149, v149 op_sel_hi:[0,0,0]
	v_mfma_scale_f32_16x16x128_f8f6f4 v[66:69], v[152:159], v[18:25], v[176:179], v149, v149 op_sel_hi:[0,0,0]
	v_mfma_scale_f32_16x16x128_f8f6f4 v[54:57], v[130:137], v[26:33], v[180:183], v149, v149 op_sel_hi:[0,0,0]
	v_mfma_scale_f32_16x16x128_f8f6f4 v[50:53], v[152:159], v[26:33], v[184:187], v149, v149 op_sel_hi:[0,0,0]
	v_mfma_scale_f32_16x16x128_f8f6f4 v[46:49], v[130:137], v[34:41], v[188:191], v149, v149 op_sel_hi:[0,0,0]
	v_mfma_scale_f32_16x16x128_f8f6f4 v[42:45], v[152:159], v[34:41], v[200:203], v149, v149 op_sel_hi:[0,0,0]
	v_mfma_scale_f32_16x16x128_f8f6f4 v[38:41], v[130:137], v[58:65], v[204:207], v149, v149 op_sel_hi:[0,0,0]
	v_mfma_scale_f32_16x16x128_f8f6f4 v[34:37], v[152:159], v[58:65], v[208:211], v149, v149 op_sel_hi:[0,0,0]
	s_setprio 0
	s_barrier
	v_mov_b32_e32 v138, v140
	ds_read_b128 v[22:25], v148 offset:49152
	ds_read_b128 v[164:167], v148 offset:51200
	ds_read_b128 v[172:175], v148 offset:53248
	ds_read_b128 v[180:183], v148 offset:55296
	v_xor_b32_e32 v148, 64, v148
	ds_read_b128 v[18:21], v148 offset:49152
	ds_read_b128 v[160:163], v148 offset:51200
	ds_read_b128 v[168:171], v148 offset:53248
	ds_read_b128 v[176:179], v148 offset:55296
	s_add_i32 s65, s65, s40
	v_lshl_add_u64 v[26:27], s[36:37], 0, v[138:139]
	v_lshl_add_u64 v[26:27], v[26:27], 0, s[6:7]
	s_mov_b32 m0, s65
	v_mov_b32_e32 v138, v142
	global_load_lds_dwordx4 v[26:27], off
	s_add_i32 m0, s65, 0x2000
	v_lshl_add_u64 v[26:27], s[36:37], 0, v[138:139]
	v_lshl_add_u64 v[26:27], v[26:27], 0, s[6:7]
	s_add_u32 s36, s36, 0x4080
	global_load_lds_dwordx4 v[26:27], off
	s_addc_u32 s37, s37, 0
	v_mov_b32_e32 v138, v1
	s_mov_b32 m0, s47
	v_lshl_add_u64 v[26:27], s[34:35], 0, v[138:139]
	v_lshl_add_u64 v[26:27], v[26:27], 0, s[6:7]
	v_mov_b32_e32 v138, v141
	global_load_lds_dwordx4 v[26:27], off
	s_mov_b32 m0, s48
	v_lshl_add_u64 v[26:27], s[34:35], 0, v[138:139]
	v_lshl_add_u64 v[26:27], v[26:27], 0, s[6:7]
	global_load_lds_dwordx4 v[26:27], off
	s_waitcnt vmcnt(6)
	s_waitcnt lgkmcnt(0)
	s_barrier
	s_setprio 1
	s_waitcnt lgkmcnt(0)
	v_mfma_scale_f32_16x16x128_f8f6f4 v[94:97], v[2:9], v[18:25], v[94:97], v149, v149 op_sel_hi:[0,0,0]
	v_mfma_scale_f32_16x16x128_f8f6f4 v[90:93], v[10:17], v[18:25], v[90:93], v149, v149 op_sel_hi:[0,0,0]
	v_mfma_scale_f32_16x16x128_f8f6f4 v[86:89], v[2:9], v[160:167], v[86:89], v149, v149 op_sel_hi:[0,0,0]
	v_mfma_scale_f32_16x16x128_f8f6f4 v[82:85], v[10:17], v[160:167], v[82:85], v149, v149 op_sel_hi:[0,0,0]
	v_mfma_scale_f32_16x16x128_f8f6f4 v[78:81], v[2:9], v[168:175], v[78:81], v149, v149 op_sel_hi:[0,0,0]
	v_mfma_scale_f32_16x16x128_f8f6f4 v[74:77], v[10:17], v[168:175], v[74:77], v149, v149 op_sel_hi:[0,0,0]
	v_mfma_scale_f32_16x16x128_f8f6f4 v[62:65], v[2:9], v[176:183], v[212:215], v149, v149 op_sel_hi:[0,0,0]
	v_mfma_scale_f32_16x16x128_f8f6f4 v[58:61], v[10:17], v[176:183], v[216:219], v149, v149 op_sel_hi:[0,0,0]
	s_setprio 0
	s_setprio 1
	v_mfma_scale_f32_16x16x128_f8f6f4 v[30:33], v[130:137], v[18:25], v[220:223], v149, v149 op_sel_hi:[0,0,0]
	v_mfma_scale_f32_16x16x128_f8f6f4 v[26:29], v[152:159], v[18:25], v[224:227], v149, v149 op_sel_hi:[0,0,0]
	v_mfma_scale_f32_16x16x128_f8f6f4 v[22:25], v[130:137], v[160:167], v[228:231], v149, v149 op_sel_hi:[0,0,0]
	v_mfma_scale_f32_16x16x128_f8f6f4 v[18:21], v[152:159], v[160:167], v[232:235], v149, v149 op_sel_hi:[0,0,0]
	v_mfma_scale_f32_16x16x128_f8f6f4 v[14:17], v[130:137], v[168:175], v[236:239], v149, v149 op_sel_hi:[0,0,0]
	v_mfma_scale_f32_16x16x128_f8f6f4 v[10:13], v[152:159], v[168:175], v[240:243], v149, v149 op_sel_hi:[0,0,0]
	v_mfma_scale_f32_16x16x128_f8f6f4 v[6:9], v[130:137], v[176:183], v[244:247], v149, v149 op_sel_hi:[0,0,0]
	v_mfma_scale_f32_16x16x128_f8f6f4 v[2:5], v[152:159], v[176:183], v[248:251], v149, v149 op_sel_hi:[0,0,0]
	s_setprio 0
	s_barrier
	s_add_i32 s64, s64, 2
	s_add_u32 s18, s18, 0x100
	s_addc_u32 s19, s19, 0
	s_add_u32 s62, s62, 0x100
	s_addc_u32 s63, s63, 0
	s_cmp_gt_u32 s64, 13
	s_cbranch_scc0 .LBB5_1678
	s_and_b64 vcc, exec, s[8:9]
	s_cbranch_vccz .LBB5_1681
	s_barrier
; #define LAS __attribute__((address_space(3)))
; __device__ __forceinline__ unsigned pk4_fp8(float a, float b, float c, float d) { int w = 0; w = __builtin_amdgcn_cvt_pk_fp8_f32(a, b, w, false); w = __builtin_amdgcn_cvt_pk_fp8_f32(c, d, w, true); return (unsigned)w; }
;     __device__ __forceinline__ void operator()(const Acc& acc, const Unit& u, int wr, int wc, int fr, int fq) const { if (u.e == 0) rs(acc, u, wr, wc, fr, fq); else cs(acc, u, wr, wc, fr, fq); }
;     __device__ __forceinline__ void operator()(const Acc& acc, const Unit& u, int wr, int wc, int fr, int fq) const {
;         const int col0 = u.pn * 256 + wc * 32 + 8 * fq; const LAS float* bl = slots + (u.idx & 1) * 512 + 256 + wc * 32 + 8 * fq;
;         f32x4 bb[2][2];
; #pragma unroll
;         for (int bj = 0; bj < 2; ++bj) { bb[bj][0] = *(const LAS f32x4*)(bl + bj * 128); bb[bj][1] = *(const LAS f32x4*)(bl + bj * 128 + 4); }
; #pragma unroll
;         for (int bj = 0; bj < 2; ++bj) { const f32x4 b0 = bb[bj][0], b1 = bb[bj][1];
; #pragma unroll
;             for (int ai = 0; ai < 2; ++ai)
; #pragma unroll
;                 for (int m = 0; m < 4; ++m) { const f32x4 v0 = acc[ai][bj][m][0] + b0, v1 = acc[ai][bj][m][1] + b1; v2u w; w.x = pk4_fp8(v0[0], v0[1], v0[2], v0[3]); w.y = pk4_fp8(v1[0], v1[1], v1[2], v1[3]);
;                     *(v2u*)(y + (size_t)EPI_ROWS(ai, m) * DM + col0 + bj * 128) = w; } }
.LBB5_1681:
	s_lshl_b32 s18, s57, 11
	s_and_b32 s18, s18, 0x800
	v_mov_b32_e32 v138, v143
	v_mov_b32_e32 v151, v144
	s_add_i32 s18, s49, s18
	s_lshl_b32 vcc_lo, s46, 2
	s_add_i32 s18, s18, vcc_lo
	v_mov_b32_e32 v162, v139
	v_lshl_add_u32 v134, v151, 6, s18
	ds_read_b128 v[152:155], v134 offset:1024
	ds_read_b128 v[156:159], v134 offset:1040
	ds_read_b128 v[130:133], v134 offset:1056
	ds_read_b128 v[134:137], v134 offset:1072
	v_mov_b32_e32 v163, v139
	s_waitcnt lgkmcnt(0)
	v_pk_add_f32 v[126:127], v[126:127], v[152:153]
	v_pk_add_f32 v[114:115], v[114:115], v[156:157]
	v_cvt_pk_fp8_f32 v162, v126, v127
	v_mov_b32_e32 v127, v139
	v_cvt_pk_fp8_f32 v127, v114, v115
	v_pk_add_f32 v[116:117], v[116:117], v[158:159]
	v_pk_add_f32 v[106:107], v[106:107], v[156:157]
	v_pk_add_f32 v[108:109], v[108:109], v[158:159]
	v_cvt_pk_fp8_f32 v127, v116, v117 op_sel:[0,0,1]
	v_mov_b32_e32 v117, v139
	v_cvt_pk_fp8_f32 v117, v106, v107
	v_pk_add_f32 v[98:99], v[98:99], v[156:157]
	v_pk_add_f32 v[100:101], v[100:101], v[158:159]
	v_pk_add_f32 v[90:91], v[90:91], v[156:157]
	v_cvt_pk_fp8_f32 v117, v108, v109 op_sel:[0,0,1]
	v_mov_b32_e32 v109, v139
	v_cvt_pk_fp8_f32 v109, v98, v99
	v_pk_add_f32 v[92:93], v[92:93], v[158:159]
	v_pk_add_f32 v[82:83], v[82:83], v[156:157]
	v_pk_add_f32 v[84:85], v[84:85], v[158:159]
	v_cvt_pk_fp8_f32 v109, v100, v101 op_sel:[0,0,1]
	v_mov_b32_e32 v101, v139
	v_cvt_pk_fp8_f32 v101, v90, v91
	v_pk_add_f32 v[74:75], v[74:75], v[156:157]
	v_pk_add_f32 v[76:77], v[76:77], v[158:159]
	v_pk_add_f32 v[58:59], v[58:59], v[156:157]
	v_cvt_pk_fp8_f32 v101, v92, v93 op_sel:[0,0,1]
	v_mov_b32_e32 v93, v139
	v_cvt_pk_fp8_f32 v93, v82, v83
	v_pk_add_f32 v[60:61], v[60:61], v[158:159]
	v_pk_add_f32 v[54:55], v[54:55], v[130:131]
	v_pk_add_f32 v[50:51], v[50:51], v[134:135]
	v_cvt_pk_fp8_f32 v93, v84, v85 op_sel:[0,0,1]
	v_mov_b32_e32 v85, v139
	v_cvt_pk_fp8_f32 v85, v74, v75
	v_pk_add_f32 v[46:47], v[46:47], v[130:131]
	v_pk_add_f32 v[42:43], v[42:43], v[134:135]
	v_pk_add_f32 v[38:39], v[38:39], v[130:131]
	v_cvt_pk_fp8_f32 v85, v76, v77 op_sel:[0,0,1]
	v_mov_b32_e32 v77, v139
	v_cvt_pk_fp8_f32 v77, v58, v59
	v_pk_add_f32 v[58:59], v[64:65], v[154:155]
	v_mov_b32_e32 v64, v139
	v_pk_add_f32 v[34:35], v[34:35], v[134:135]
	v_cvt_pk_fp8_f32 v77, v60, v61 op_sel:[0,0,1]
	v_pk_add_f32 v[60:61], v[70:71], v[130:131]
	v_pk_add_f32 v[30:31], v[30:31], v[130:131]
	v_cvt_pk_fp8_f32 v64, v60, v61
	v_pk_add_f32 v[60:61], v[72:73], v[132:133]
	v_pk_add_f32 v[26:27], v[26:27], v[134:135]
	v_pk_add_f32 v[22:23], v[22:23], v[130:131]
	v_cvt_pk_fp8_f32 v64, v60, v61 op_sel:[0,0,1]
	v_mov_b32_e32 v60, v139
	v_cvt_pk_fp8_f32 v60, v54, v55
	v_mov_b32_e32 v61, v139
	v_cvt_pk_fp8_f32 v61, v50, v51
	v_pk_add_f32 v[50:51], v[56:57], v[132:133]
	v_pk_add_f32 v[18:19], v[18:19], v[134:135]
	v_cvt_pk_fp8_f32 v60, v50, v51 op_sel:[0,0,1]
	v_mov_b32_e32 v50, v139
	v_cvt_pk_fp8_f32 v50, v46, v47
	v_mov_b32_e32 v51, v139
	v_cvt_pk_fp8_f32 v51, v42, v43
	v_pk_add_f32 v[42:43], v[48:49], v[132:133]
	v_pk_add_f32 v[122:123], v[122:123], v[156:157]
	v_cvt_pk_fp8_f32 v50, v42, v43 op_sel:[0,0,1]
	v_mov_b32_e32 v42, v139
	v_cvt_pk_fp8_f32 v42, v38, v39
	v_mov_b32_e32 v43, v139
	v_cvt_pk_fp8_f32 v43, v34, v35
	v_pk_add_f32 v[34:35], v[40:41], v[132:133]
	v_pk_add_f32 v[14:15], v[14:15], v[130:131]
	v_cvt_pk_fp8_f32 v42, v34, v35 op_sel:[0,0,1]
	v_mov_b32_e32 v34, v139
	v_cvt_pk_fp8_f32 v34, v30, v31
	v_mov_b32_e32 v35, v139
	v_cvt_pk_fp8_f32 v35, v26, v27
	v_pk_add_f32 v[26:27], v[32:33], v[132:133]
	v_cvt_pk_fp8_f32 v163, v122, v123
	v_cvt_pk_fp8_f32 v34, v26, v27 op_sel:[0,0,1]
	v_mov_b32_e32 v26, v139
	v_cvt_pk_fp8_f32 v26, v22, v23
	v_mov_b32_e32 v27, v139
	v_cvt_pk_fp8_f32 v27, v18, v19
	v_pk_add_f32 v[18:19], v[24:25], v[132:133]
	v_pk_add_f32 v[118:119], v[118:119], v[152:153]
	v_cvt_pk_fp8_f32 v26, v18, v19 op_sel:[0,0,1]
	v_mov_b32_e32 v18, v139
	v_mov_b32_e32 v126, v139
	v_pk_add_f32 v[110:111], v[110:111], v[152:153]
	v_mov_b32_e32 v116, v139
	v_pk_add_f32 v[102:103], v[102:103], v[152:153]
	v_mov_b32_e32 v108, v139
	v_pk_add_f32 v[94:95], v[94:95], v[152:153]
	v_mov_b32_e32 v100, v139
	v_pk_add_f32 v[86:87], v[86:87], v[152:153]
	v_mov_b32_e32 v92, v139
	v_pk_add_f32 v[78:79], v[78:79], v[152:153]
	v_mov_b32_e32 v84, v139
	v_pk_add_f32 v[62:63], v[62:63], v[152:153]
	v_mov_b32_e32 v76, v139
	v_cvt_pk_fp8_f32 v18, v14, v15
	v_cvt_pk_fp8_f32 v126, v118, v119
	v_cvt_pk_fp8_f32 v116, v110, v111
	v_cvt_pk_fp8_f32 v108, v102, v103
	v_cvt_pk_fp8_f32 v100, v94, v95
	v_cvt_pk_fp8_f32 v92, v86, v87
	v_cvt_pk_fp8_f32 v84, v78, v79
	v_cvt_pk_fp8_f32 v76, v62, v63
	v_pk_add_f32 v[62:63], v[66:67], v[134:135]
	v_mov_b32_e32 v65, v139
	s_lshl_b32 s11, s11, 8
	v_cvt_pk_fp8_f32 v65, v62, v63
	v_pk_add_f32 v[10:11], v[10:11], v[134:135]
	v_mov_b32_e32 v19, v139
	v_pk_add_f32 v[124:125], v[124:125], v[158:159]
	s_add_i32 s11, s11, s45
	v_cvt_pk_fp8_f32 v19, v10, v11
	v_pk_add_f32 v[10:11], v[16:17], v[132:133]
	v_cvt_pk_fp8_f32 v163, v124, v125 op_sel:[0,0,1]
	v_add_u32_e32 v124, s11, v138
	v_pk_add_f32 v[114:115], v[120:121], v[154:155]
	v_pk_add_f32 v[106:107], v[112:113], v[154:155]
	v_pk_add_f32 v[98:99], v[104:105], v[154:155]
	v_pk_add_f32 v[90:91], v[96:97], v[154:155]
	v_pk_add_f32 v[82:83], v[88:89], v[154:155]
	v_pk_add_f32 v[74:75], v[80:81], v[154:155]
; #define LAS __attribute__((address_space(3)))
; __device__ __forceinline__ unsigned pk4_fp8(float a, float b, float c, float d) { int w = 0; w = __builtin_amdgcn_cvt_pk_fp8_f32(a, b, w, false); w = __builtin_amdgcn_cvt_pk_fp8_f32(c, d, w, true); return (unsigned)w; }
;     __device__ __forceinline__ void prefetch(const Unit& u) const { if (u.e == 0) rs.prefetch(u); else cs.prefetch(u); }
;     __device__ __forceinline__ void prefetch(const Unit& u) const { const int tid = threadIdx.x, w = __builtin_amdgcn_readfirstlane(tid >> 6);
;         if (w < 4) __builtin_amdgcn_global_load_lds((const unsigned*)(b_dn + (size_t)u.e * DM + u.pn * 256 + tid), (LAS unsigned*)(slots + (u.idx & 1) * 512 + 256 + w * 64), 4, 0, 0); }
;     __device__ __forceinline__ void operator()(const Acc& acc, const Unit& u, int wr, int wc, int fr, int fq) const {
;         const int col0 = u.pn * 256 + wc * 32 + 8 * fq; const LAS float* bl = slots + (u.idx & 1) * 512 + 256 + wc * 32 + 8 * fq;
;         f32x4 bb[2][2];
; #pragma unroll
;         for (int bj = 0; bj < 2; ++bj) { bb[bj][0] = *(const LAS f32x4*)(bl + bj * 128); bb[bj][1] = *(const LAS f32x4*)(bl + bj * 128 + 4); }
; #pragma unroll
;         for (int bj = 0; bj < 2; ++bj) { const f32x4 b0 = bb[bj][0], b1 = bb[bj][1];
; #pragma unroll
;             for (int ai = 0; ai < 2; ++ai)
; #pragma unroll
;                 for (int m = 0; m < 4; ++m) { const f32x4 v0 = acc[ai][bj][m][0] + b0, v1 = acc[ai][bj][m][1] + b1; v2u w; w.x = pk4_fp8(v0[0], v0[1], v0[2], v0[3]); w.y = pk4_fp8(v1[0], v1[1], v1[2], v1[3]);
;                     *(v2u*)(y + (size_t)EPI_ROWS(ai, m) * DM + col0 + bj * 128) = w; } }
	v_cvt_pk_fp8_f32 v18, v10, v11 op_sel:[0,0,1]
	v_pk_add_f32 v[6:7], v[6:7], v[130:131]
	v_pk_add_f32 v[2:3], v[2:3], v[134:135]
	v_mov_b32_e32 v10, v139
	v_mov_b32_e32 v11, v139
	s_lshl_b32 s18, s56, 8
	v_pk_add_f32 v[122:123], v[128:129], v[154:155]
	v_cvt_pk_fp8_f32 v126, v114, v115 op_sel:[0,0,1]
	v_add_u32_e32 v114, 16, v124
	v_cvt_pk_fp8_f32 v116, v106, v107 op_sel:[0,0,1]
	v_add_u32_e32 v106, 32, v124
	v_cvt_pk_fp8_f32 v108, v98, v99 op_sel:[0,0,1]
	v_add_u32_e32 v98, 48, v124
	v_cvt_pk_fp8_f32 v100, v90, v91 op_sel:[0,0,1]
	v_add_u32_e32 v90, 0x80, v124
	v_cvt_pk_fp8_f32 v92, v82, v83 op_sel:[0,0,1]
	v_add_u32_e32 v82, 0x90, v124
	v_cvt_pk_fp8_f32 v84, v74, v75 op_sel:[0,0,1]
	v_add_u32_e32 v74, 0xa0, v124
	v_cvt_pk_fp8_f32 v76, v58, v59 op_sel:[0,0,1]
	v_add_u32_e32 v58, 0xb0, v124
	v_pk_add_f32 v[62:63], v[68:69], v[136:137]
	v_pk_add_f32 v[28:29], v[28:29], v[136:137]
	v_cvt_pk_fp8_f32 v10, v6, v7
	v_cvt_pk_fp8_f32 v11, v2, v3
	s_add_i32 s18, s18, s46
	s_add_i32 s18, s18, s46
	v_cvt_pk_fp8_f32 v162, v122, v123 op_sel:[0,0,1]
	v_ashrrev_i32_e32 v125, 31, v124
	v_ashrrev_i32_e32 v115, 31, v114
	v_ashrrev_i32_e32 v107, 31, v106
	v_ashrrev_i32_e32 v99, 31, v98
	v_ashrrev_i32_e32 v91, 31, v90
	v_ashrrev_i32_e32 v83, 31, v82
	v_ashrrev_i32_e32 v75, 31, v74
	v_ashrrev_i32_e32 v59, 31, v58
	v_cvt_pk_fp8_f32 v65, v62, v63 op_sel:[0,0,1]
	v_pk_add_f32 v[52:53], v[52:53], v[136:137]
	v_cvt_pk_fp8_f32 v35, v28, v29 op_sel:[0,0,1]
	v_pk_add_f32 v[20:21], v[20:21], v[136:137]
	v_lshl_add_u32 v160, v151, 4, s18
	v_lshlrev_b64 v[122:123], 11, v[124:125]
	v_lshlrev_b64 v[114:115], 11, v[114:115]
	v_lshlrev_b64 v[106:107], 11, v[106:107]
	v_lshlrev_b64 v[98:99], 11, v[98:99]
	v_lshlrev_b64 v[90:91], 11, v[90:91]
	v_lshlrev_b64 v[82:83], 11, v[82:83]
	v_lshlrev_b64 v[74:75], 11, v[74:75]
	v_lshlrev_b64 v[58:59], 11, v[58:59]
	v_cvt_pk_fp8_f32 v61, v52, v53 op_sel:[0,0,1]
	v_pk_add_f32 v[44:45], v[44:45], v[136:137]
	v_cvt_pk_fp8_f32 v27, v20, v21 op_sel:[0,0,1]
	v_pk_add_f32 v[12:13], v[12:13], v[136:137]
	v_ashrrev_i32_e32 v161, 31, v160
	v_lshl_add_u64 v[122:123], s[4:5], 0, v[122:123]
	v_lshl_add_u64 v[114:115], s[4:5], 0, v[114:115]
	v_lshl_add_u64 v[106:107], s[4:5], 0, v[106:107]
	v_lshl_add_u64 v[98:99], s[4:5], 0, v[98:99]
	v_lshl_add_u64 v[90:91], s[4:5], 0, v[90:91]
	v_lshl_add_u64 v[82:83], s[4:5], 0, v[82:83]
	v_lshl_add_u64 v[74:75], s[4:5], 0, v[74:75]
	v_lshl_add_u64 v[58:59], s[4:5], 0, v[58:59]
	v_cvt_pk_fp8_f32 v51, v44, v45 op_sel:[0,0,1]
	v_pk_add_f32 v[36:37], v[36:37], v[136:137]
	v_cvt_pk_fp8_f32 v19, v12, v13 op_sel:[0,0,1]
	v_pk_add_f32 v[2:3], v[8:9], v[132:133]
	v_pk_add_f32 v[4:5], v[4:5], v[136:137]
	v_lshl_add_u64 v[122:123], v[122:123], 0, v[160:161]
	v_lshl_add_u64 v[114:115], v[114:115], 0, v[160:161]
	v_lshl_add_u64 v[106:107], v[106:107], 0, v[160:161]
	v_lshl_add_u64 v[98:99], v[98:99], 0, v[160:161]
	v_lshl_add_u64 v[90:91], v[90:91], 0, v[160:161]
	v_lshl_add_u64 v[82:83], v[82:83], 0, v[160:161]
	v_lshl_add_u64 v[74:75], v[74:75], 0, v[160:161]
	v_lshl_add_u64 v[58:59], v[58:59], 0, v[160:161]
	v_cvt_pk_fp8_f32 v43, v36, v37 op_sel:[0,0,1]
	v_cvt_pk_fp8_f32 v10, v2, v3 op_sel:[0,0,1]
	v_cvt_pk_fp8_f32 v11, v4, v5 op_sel:[0,0,1]
	s_andn2_b64 vcc, exec, s[16:17]
	s_mov_b64 s[16:17], -1
	v_mov_b32_e32 v244, v162
	v_mov_b32_e32 v245, v163
	v_mov_b32_e32 v246, v64
	v_mov_b32_e32 v247, v65
	global_store_dwordx4 v[122:123], v[244:247], off
	v_mov_b32_e32 v248, v126
	v_mov_b32_e32 v249, v127
	v_mov_b32_e32 v250, v60
	v_mov_b32_e32 v251, v61
	global_store_dwordx4 v[114:115], v[248:251], off
	v_mov_b32_e32 v244, v116
	v_mov_b32_e32 v245, v117
	v_mov_b32_e32 v246, v50
	v_mov_b32_e32 v247, v51
	global_store_dwordx4 v[106:107], v[244:247], off
	v_mov_b32_e32 v248, v108
	v_mov_b32_e32 v249, v109
	v_mov_b32_e32 v250, v42
	v_mov_b32_e32 v251, v43
	global_store_dwordx4 v[98:99], v[248:251], off
	v_mov_b32_e32 v244, v100
	v_mov_b32_e32 v245, v101
	v_mov_b32_e32 v246, v34
	v_mov_b32_e32 v247, v35
	global_store_dwordx4 v[90:91], v[244:247], off
	v_mov_b32_e32 v248, v92
	v_mov_b32_e32 v249, v93
	v_mov_b32_e32 v250, v26
	v_mov_b32_e32 v251, v27
	global_store_dwordx4 v[82:83], v[248:251], off
	v_mov_b32_e32 v244, v84
	v_mov_b32_e32 v245, v85
	v_mov_b32_e32 v246, v18
	v_mov_b32_e32 v247, v19
	global_store_dwordx4 v[74:75], v[244:247], off
	v_mov_b32_e32 v248, v76
	v_mov_b32_e32 v249, v77
	v_mov_b32_e32 v250, v10
	v_mov_b32_e32 v251, v11
	global_store_dwordx4 v[58:59], v[248:251], off
	s_cbranch_vccnz .LBB5_1672
	v_readfirstlane_b32 s11, v0
	s_cmpk_gt_u32 s11, 0xff
	s_cbranch_scc1 .LBB5_1684
	v_readlane_b32 s56, v253, 2
	s_and_b32 s18, s11, 0xc0
	s_ashr_i32 s11, s10, 31
	v_readlane_b32 s57, v253, 3
	v_readlane_b32 s58, v253, 4
	v_readlane_b32 s59, v253, 5
	v_readlane_b32 s60, v253, 6
	v_readlane_b32 s61, v253, 7
	s_lshl_b64 s[16:17], s[10:11], 13
	v_readlane_b32 s62, v253, 8
	v_readlane_b32 s63, v253, 9
	s_mov_b64 s[56:57], s[60:61]
	s_add_u32 s11, s56, s16
	s_addc_u32 s19, s57, s17
	s_lshl_b32 s16, s52, 8
	s_ashr_i32 s17, s16, 31
	s_lshl_b64 s[16:17], s[16:17], 2
	s_add_u32 s16, s11, s16
	s_addc_u32 s17, s19, s17
	s_lshl_b32 s11, s55, 11
	s_and_b32 s11, s11, 0x800
	s_add_i32 s11, s11, 0
	s_lshl_b32 s18, s18, 2
	s_add_i32 s11, s11, s18
	s_add_i32 m0, s11, 0x20c00
	s_mov_b64 s[58:59], s[62:63]
	global_load_lds_dword v150, s[16:17]
